# ordered-emission pass: the last key of groups 0-2 also made branch-free (8 instructions instead of a 35-line branchy block plus 3 state-conversion instructions)
# speedup vs baseline: 1.0018x; 1.0018x over previous
.LBB0_718:
	v_lshl_add_u64 v[8:9], v[6:7], 1, s[12:13]
	global_load_dwordx4 v[4:7], v[8:9], off offset:16
	s_nop 0
	global_load_dwordx4 v[8:11], v[8:9], off
	s_and_saveexec_b64 s[24:25], vcc
	s_cbranch_execz .LBB0_845
	ds_read_u16 v2, v49 offset:36864
	v_add_u32_e32 v44, 0x11200, v49
	ds_read_b32 v44, v44
	s_waitcnt vmcnt(6)
	s_waitcnt lgkmcnt(1)
	v_lshrrev_b32_e32 v45, 8, v2
	v_and_b32_e32 v2, 0xff, v2
	v_cndmask_b32_e64 v45, v45, 0, s[22:23]
	v_cndmask_b32_e64 v2, v2, 0, s[22:23]
	s_waitcnt lgkmcnt(0)
	v_add_u32_sdwa v51, v45, v44 dst_sel:DWORD dst_unused:UNUSED_PAD src0_sel:DWORD src1_sel:WORD_1
	v_add_u32_sdwa v214, v2, v44 dst_sel:DWORD dst_unused:UNUSED_PAD src0_sel:DWORD src1_sel:WORD_0
	v_lshl_add_u64 v[44:45], v[40:41], 0, s[16:17]
	v_min_i32_e32 v2, v51, v37
	v_add_u32_e32 v2, v2, v214
	v_sub_u32_e32 v51, v37, v51
	v_med3_i32 v214, v51, 0, 1
	v_sub_u32_e32 v214, v36, v214
	v_cmp_gt_i32_sdwa s[0:1], v32, v214 src0_sel:WORD_0 src1_sel:DWORD
	v_cmp_eq_u32_sdwa s[30:31], v32, v36 src0_sel:WORD_0 src1_sel:DWORD
	v_lshl_add_u64 v[46:47], v[2:3], 1, v[38:39]
	s_and_saveexec_b64 s[34:35], s[0:1]
	global_store_short v[46:47], v44, off
	s_mov_b64 exec, s[34:35]
	v_addc_co_u32_e64 v2, vcc, 0, v2, s[0:1]
	v_subb_co_u32_e64 v51, vcc, v51, 0, s[30:31]
	v_lshl_add_u64 v[46:47], v[44:45], 0, 1
	v_med3_i32 v214, v51, 0, 1
	v_sub_u32_e32 v214, v36, v214
	v_cmp_gt_i32_sdwa s[0:1], v32, v214 src0_sel:WORD_1 src1_sel:DWORD
	v_cmp_eq_u32_sdwa s[30:31], v32, v36 src0_sel:WORD_1 src1_sel:DWORD
	v_lshl_add_u64 v[212:213], v[2:3], 1, v[38:39]
	s_and_saveexec_b64 s[34:35], s[0:1]
	global_store_short v[212:213], v46, off
	s_mov_b64 exec, s[34:35]
	v_addc_co_u32_e64 v2, vcc, 0, v2, s[0:1]
	v_subb_co_u32_e64 v51, vcc, v51, 0, s[30:31]
	v_lshl_add_u64 v[46:47], v[44:45], 0, 2
	v_med3_i32 v214, v51, 0, 1
	v_sub_u32_e32 v214, v36, v214
	v_cmp_gt_i32_sdwa s[0:1], v33, v214 src0_sel:WORD_0 src1_sel:DWORD
	v_cmp_eq_u32_sdwa s[30:31], v33, v36 src0_sel:WORD_0 src1_sel:DWORD
	v_lshl_add_u64 v[212:213], v[2:3], 1, v[38:39]
	s_and_saveexec_b64 s[34:35], s[0:1]
	global_store_short v[212:213], v46, off
	s_mov_b64 exec, s[34:35]
	v_addc_co_u32_e64 v2, vcc, 0, v2, s[0:1]
	v_subb_co_u32_e64 v51, vcc, v51, 0, s[30:31]
	v_lshl_add_u64 v[46:47], v[44:45], 0, 3
	v_med3_i32 v214, v51, 0, 1
	v_sub_u32_e32 v214, v36, v214
	v_cmp_gt_i32_sdwa s[0:1], v33, v214 src0_sel:WORD_1 src1_sel:DWORD
	v_cmp_eq_u32_sdwa s[30:31], v33, v36 src0_sel:WORD_1 src1_sel:DWORD
	v_lshl_add_u64 v[32:33], v[2:3], 1, v[38:39]
	s_and_saveexec_b64 s[34:35], s[0:1]
	global_store_short v[32:33], v46, off
	s_mov_b64 exec, s[34:35]
	v_addc_co_u32_e64 v2, vcc, 0, v2, s[0:1]
	v_subb_co_u32_e64 v51, vcc, v51, 0, s[30:31]
	v_lshl_add_u64 v[32:33], v[44:45], 0, 4
	v_med3_i32 v214, v51, 0, 1
	v_sub_u32_e32 v214, v36, v214
	v_cmp_gt_i32_sdwa s[0:1], v34, v214 src0_sel:WORD_0 src1_sel:DWORD
	v_cmp_eq_u32_sdwa s[30:31], v34, v36 src0_sel:WORD_0 src1_sel:DWORD
	v_lshl_add_u64 v[46:47], v[2:3], 1, v[38:39]
	s_and_saveexec_b64 s[34:35], s[0:1]
	global_store_short v[46:47], v32, off
	s_mov_b64 exec, s[34:35]
	v_addc_co_u32_e64 v2, vcc, 0, v2, s[0:1]
	v_subb_co_u32_e64 v51, vcc, v51, 0, s[30:31]
	v_lshl_add_u64 v[32:33], v[44:45], 0, 5
	v_med3_i32 v214, v51, 0, 1
	v_sub_u32_e32 v214, v36, v214
	v_cmp_gt_i32_sdwa s[0:1], v34, v214 src0_sel:WORD_1 src1_sel:DWORD
	v_cmp_eq_u32_sdwa s[30:31], v34, v36 src0_sel:WORD_1 src1_sel:DWORD
	v_lshl_add_u64 v[46:47], v[2:3], 1, v[38:39]
	s_and_saveexec_b64 s[34:35], s[0:1]
	global_store_short v[46:47], v32, off
	s_mov_b64 exec, s[34:35]
	v_addc_co_u32_e64 v2, vcc, 0, v2, s[0:1]
	v_subb_co_u32_e64 v51, vcc, v51, 0, s[30:31]
	v_lshl_add_u64 v[32:33], v[44:45], 0, 6
	v_med3_i32 v214, v51, 0, 1
	v_sub_u32_e32 v214, v36, v214
	v_cmp_gt_i32_sdwa s[0:1], v35, v214 src0_sel:WORD_0 src1_sel:DWORD
	v_cmp_eq_u32_sdwa s[30:31], v35, v36 src0_sel:WORD_0 src1_sel:DWORD
	v_lshl_add_u64 v[46:47], v[2:3], 1, v[38:39]
	s_and_saveexec_b64 s[34:35], s[0:1]
	global_store_short v[46:47], v32, off
	s_mov_b64 exec, s[34:35]
	v_addc_co_u32_e64 v2, vcc, 0, v2, s[0:1]
	v_subb_co_u32_e64 v51, vcc, v51, 0, s[30:31]
	v_lshl_add_u64 v[32:33], v[44:45], 0, 7
	v_med3_i32 v214, v51, 0, 1
	v_sub_u32_e32 v214, v36, v214
	v_cmp_gt_i32_sdwa s[0:1], v35, v214 src0_sel:WORD_1 src1_sel:DWORD
	v_cmp_eq_u32_sdwa s[30:31], v35, v36 src0_sel:WORD_1 src1_sel:DWORD
	v_lshl_add_u64 v[34:35], v[2:3], 1, v[38:39]
	s_and_saveexec_b64 s[34:35], s[0:1]
	global_store_short v[34:35], v32, off
	s_mov_b64 exec, s[34:35]
	v_addc_co_u32_e64 v2, vcc, 0, v2, s[0:1]
	v_subb_co_u32_e64 v51, vcc, v51, 0, s[30:31]
	v_lshl_add_u64 v[32:33], v[44:45], 0, 8
	v_med3_i32 v214, v51, 0, 1
	v_sub_u32_e32 v214, v36, v214
	v_cmp_gt_i32_sdwa s[0:1], v28, v214 src0_sel:WORD_0 src1_sel:DWORD
	v_cmp_eq_u32_sdwa s[30:31], v28, v36 src0_sel:WORD_0 src1_sel:DWORD
	v_lshl_add_u64 v[34:35], v[2:3], 1, v[38:39]
	s_and_saveexec_b64 s[34:35], s[0:1]
	global_store_short v[34:35], v32, off
	s_mov_b64 exec, s[34:35]
	v_addc_co_u32_e64 v2, vcc, 0, v2, s[0:1]
	v_subb_co_u32_e64 v51, vcc, v51, 0, s[30:31]
	v_lshl_add_u64 v[32:33], v[44:45], 0, 9
	v_med3_i32 v214, v51, 0, 1
	v_sub_u32_e32 v214, v36, v214
	v_cmp_gt_i32_sdwa s[0:1], v28, v214 src0_sel:WORD_1 src1_sel:DWORD
	v_cmp_eq_u32_sdwa s[30:31], v28, v36 src0_sel:WORD_1 src1_sel:DWORD
	v_lshl_add_u64 v[34:35], v[2:3], 1, v[38:39]
	s_and_saveexec_b64 s[34:35], s[0:1]
	global_store_short v[34:35], v32, off
	s_mov_b64 exec, s[34:35]
	v_addc_co_u32_e64 v2, vcc, 0, v2, s[0:1]
	v_subb_co_u32_e64 v51, vcc, v51, 0, s[30:31]
	v_lshl_add_u64 v[32:33], v[44:45], 0, 10
	v_med3_i32 v214, v51, 0, 1
	v_sub_u32_e32 v214, v36, v214
	v_cmp_gt_i32_sdwa s[0:1], v29, v214 src0_sel:WORD_0 src1_sel:DWORD
	v_cmp_eq_u32_sdwa s[30:31], v29, v36 src0_sel:WORD_0 src1_sel:DWORD
	v_lshl_add_u64 v[34:35], v[2:3], 1, v[38:39]
	s_and_saveexec_b64 s[34:35], s[0:1]
	global_store_short v[34:35], v32, off
	s_mov_b64 exec, s[34:35]
	v_addc_co_u32_e64 v2, vcc, 0, v2, s[0:1]
	v_subb_co_u32_e64 v51, vcc, v51, 0, s[30:31]
	v_lshl_add_u64 v[32:33], v[44:45], 0, 11
	v_med3_i32 v214, v51, 0, 1
	v_sub_u32_e32 v214, v36, v214
	v_cmp_gt_i32_sdwa s[0:1], v29, v214 src0_sel:WORD_1 src1_sel:DWORD
	v_cmp_eq_u32_sdwa s[30:31], v29, v36 src0_sel:WORD_1 src1_sel:DWORD
	v_lshl_add_u64 v[28:29], v[2:3], 1, v[38:39]
	s_and_saveexec_b64 s[34:35], s[0:1]
	global_store_short v[28:29], v32, off
	s_mov_b64 exec, s[34:35]
	v_addc_co_u32_e64 v2, vcc, 0, v2, s[0:1]
	v_subb_co_u32_e64 v51, vcc, v51, 0, s[30:31]
	v_lshl_add_u64 v[28:29], v[44:45], 0, 12
	v_med3_i32 v214, v51, 0, 1
	v_sub_u32_e32 v214, v36, v214
	v_cmp_gt_i32_sdwa s[0:1], v30, v214 src0_sel:WORD_0 src1_sel:DWORD
	v_cmp_eq_u32_sdwa s[30:31], v30, v36 src0_sel:WORD_0 src1_sel:DWORD
	v_lshl_add_u64 v[32:33], v[2:3], 1, v[38:39]
	s_and_saveexec_b64 s[34:35], s[0:1]
	global_store_short v[32:33], v28, off
	s_mov_b64 exec, s[34:35]
	v_addc_co_u32_e64 v2, vcc, 0, v2, s[0:1]
	v_subb_co_u32_e64 v51, vcc, v51, 0, s[30:31]
	v_lshl_add_u64 v[28:29], v[44:45], 0, 13
	v_med3_i32 v214, v51, 0, 1
	v_sub_u32_e32 v214, v36, v214
	v_cmp_gt_i32_sdwa s[0:1], v30, v214 src0_sel:WORD_1 src1_sel:DWORD
	v_cmp_eq_u32_sdwa s[30:31], v30, v36 src0_sel:WORD_1 src1_sel:DWORD
	v_lshl_add_u64 v[32:33], v[2:3], 1, v[38:39]
	s_and_saveexec_b64 s[34:35], s[0:1]
	global_store_short v[32:33], v28, off
	s_mov_b64 exec, s[34:35]
	v_addc_co_u32_e64 v2, vcc, 0, v2, s[0:1]
	v_subb_co_u32_e64 v51, vcc, v51, 0, s[30:31]
	v_lshl_add_u64 v[28:29], v[44:45], 0, 14
	v_med3_i32 v214, v51, 0, 1
	v_sub_u32_e32 v214, v36, v214
	v_cmp_gt_i32_sdwa s[0:1], v31, v214 src0_sel:WORD_0 src1_sel:DWORD
	v_cmp_eq_u32_sdwa s[30:31], v31, v36 src0_sel:WORD_0 src1_sel:DWORD
	v_lshl_add_u64 v[32:33], v[2:3], 1, v[38:39]
	s_and_saveexec_b64 s[34:35], s[0:1]
	global_store_short v[32:33], v28, off
	s_mov_b64 exec, s[34:35]
	v_addc_co_u32_e64 v2, vcc, 0, v2, s[0:1]
	v_subb_co_u32_e64 v51, vcc, v51, 0, s[30:31]
	v_med3_i32 v214, v51, 0, 1
	v_sub_u32_e32 v214, v36, v214
	v_cmp_gt_i32_sdwa s[30:31], v31, v214 src0_sel:WORD_1 src1_sel:DWORD
	v_lshl_add_u64 v[28:29], v[2:3], 1, v[38:39]
	v_or_b32_e32 v214, 15, v44
	s_and_saveexec_b64 s[34:35], s[30:31]
	global_store_short v[28:29], v214, off
	s_mov_b64 exec, s[34:35]
.LBB0_843:
.LBB0_844:
.LBB0_845:
	s_or_b64 exec, exec, s[24:25]
	s_andn2_b64 vcc, exec, s[18:19]
	s_cbranch_vccnz .LBB0_975
	ds_read_u16 v2, v50 offset:36896
	s_waitcnt lgkmcnt(0)
	v_cmp_ne_u16_e32 vcc, 0, v2
	s_and_saveexec_b64 s[18:19], vcc
	s_cbranch_execz .LBB0_973
	ds_read_u16 v2, v49 offset:36896
	s_waitcnt vmcnt(7)
	v_add_u32_e32 v28, 0x11220, v49
	ds_read_b32 v28, v28
	v_lshl_add_u64 v[30:31], v[40:41], 0, s[16:17]
	s_waitcnt vmcnt(4)
	s_waitcnt lgkmcnt(1)
	v_lshrrev_b32_e32 v29, 8, v2
	v_and_b32_e32 v2, 0xff, v2
	v_cndmask_b32_e64 v29, v29, 0, s[22:23]
	v_cndmask_b32_e64 v2, v2, 0, s[22:23]
	s_waitcnt lgkmcnt(0)
	v_add_u32_sdwa v34, v29, v28 dst_sel:DWORD dst_unused:UNUSED_PAD src0_sel:DWORD src1_sel:WORD_1
	v_add_u32_sdwa v35, v2, v28 dst_sel:DWORD dst_unused:UNUSED_PAD src0_sel:DWORD src1_sel:WORD_0
	v_lshl_add_u64 v[28:29], v[30:31], 0, s[84:85]
	v_min_i32_e32 v2, v34, v37
	v_add_u32_e32 v2, v2, v35
	v_sub_u32_e32 v34, v37, v34
	v_med3_i32 v35, v34, 0, 1
	v_sub_u32_e32 v35, v36, v35
	v_cmp_gt_i32_sdwa s[0:1], v24, v35 src0_sel:WORD_0 src1_sel:DWORD
	v_cmp_eq_u32_sdwa s[24:25], v24, v36 src0_sel:WORD_0 src1_sel:DWORD
	v_lshl_add_u64 v[32:33], v[2:3], 1, v[38:39]
	s_and_saveexec_b64 s[30:31], s[0:1]
	global_store_short v[32:33], v28, off
	s_mov_b64 exec, s[30:31]
	v_addc_co_u32_e64 v2, vcc, 0, v2, s[0:1]
	v_subb_co_u32_e64 v34, vcc, v34, 0, s[24:25]
	v_add_u32_e32 v32, 0x101, v30
	v_med3_i32 v35, v34, 0, 1
	v_sub_u32_e32 v35, v36, v35
	v_cmp_gt_i32_sdwa s[0:1], v24, v35 src0_sel:WORD_1 src1_sel:DWORD
	v_cmp_eq_u32_sdwa s[24:25], v24, v36 src0_sel:WORD_1 src1_sel:DWORD
	v_lshl_add_u64 v[44:45], v[2:3], 1, v[38:39]
	s_and_saveexec_b64 s[30:31], s[0:1]
	global_store_short v[44:45], v32, off
	s_mov_b64 exec, s[30:31]
	v_addc_co_u32_e64 v2, vcc, 0, v2, s[0:1]
	v_subb_co_u32_e64 v34, vcc, v34, 0, s[24:25]
	v_add_u32_e32 v32, 0x102, v30
	v_med3_i32 v35, v34, 0, 1
	v_sub_u32_e32 v35, v36, v35
	v_cmp_gt_i32_sdwa s[0:1], v25, v35 src0_sel:WORD_0 src1_sel:DWORD
	v_cmp_eq_u32_sdwa s[24:25], v25, v36 src0_sel:WORD_0 src1_sel:DWORD
	v_lshl_add_u64 v[44:45], v[2:3], 1, v[38:39]
	s_and_saveexec_b64 s[30:31], s[0:1]
	global_store_short v[44:45], v32, off
	s_mov_b64 exec, s[30:31]
	v_addc_co_u32_e64 v2, vcc, 0, v2, s[0:1]
	v_subb_co_u32_e64 v34, vcc, v34, 0, s[24:25]
	v_add_u32_e32 v32, 0x103, v30
	v_med3_i32 v35, v34, 0, 1
	v_sub_u32_e32 v35, v36, v35
	v_cmp_gt_i32_sdwa s[0:1], v25, v35 src0_sel:WORD_1 src1_sel:DWORD
	v_cmp_eq_u32_sdwa s[24:25], v25, v36 src0_sel:WORD_1 src1_sel:DWORD
	v_lshl_add_u64 v[24:25], v[2:3], 1, v[38:39]
	s_and_saveexec_b64 s[30:31], s[0:1]
	global_store_short v[24:25], v32, off
	s_mov_b64 exec, s[30:31]
	v_addc_co_u32_e64 v2, vcc, 0, v2, s[0:1]
	v_subb_co_u32_e64 v34, vcc, v34, 0, s[24:25]
	v_add_u32_e32 v24, 0x104, v30
	v_med3_i32 v35, v34, 0, 1
	v_sub_u32_e32 v35, v36, v35
	v_cmp_gt_i32_sdwa s[0:1], v26, v35 src0_sel:WORD_0 src1_sel:DWORD
	v_cmp_eq_u32_sdwa s[24:25], v26, v36 src0_sel:WORD_0 src1_sel:DWORD
	v_lshl_add_u64 v[32:33], v[2:3], 1, v[38:39]
	s_and_saveexec_b64 s[30:31], s[0:1]
	global_store_short v[32:33], v24, off
	s_mov_b64 exec, s[30:31]
	v_addc_co_u32_e64 v2, vcc, 0, v2, s[0:1]
	v_subb_co_u32_e64 v34, vcc, v34, 0, s[24:25]
	v_add_u32_e32 v24, 0x105, v30
	v_med3_i32 v35, v34, 0, 1
	v_sub_u32_e32 v35, v36, v35
	v_cmp_gt_i32_sdwa s[0:1], v26, v35 src0_sel:WORD_1 src1_sel:DWORD
	v_cmp_eq_u32_sdwa s[24:25], v26, v36 src0_sel:WORD_1 src1_sel:DWORD
	v_lshl_add_u64 v[32:33], v[2:3], 1, v[38:39]
	s_and_saveexec_b64 s[30:31], s[0:1]
	global_store_short v[32:33], v24, off
	s_mov_b64 exec, s[30:31]
	v_addc_co_u32_e64 v2, vcc, 0, v2, s[0:1]
	v_subb_co_u32_e64 v34, vcc, v34, 0, s[24:25]
	v_add_u32_e32 v24, 0x106, v30
	v_med3_i32 v35, v34, 0, 1
	v_sub_u32_e32 v35, v36, v35
	v_cmp_gt_i32_sdwa s[0:1], v27, v35 src0_sel:WORD_0 src1_sel:DWORD
	v_cmp_eq_u32_sdwa s[24:25], v27, v36 src0_sel:WORD_0 src1_sel:DWORD
	v_lshl_add_u64 v[32:33], v[2:3], 1, v[38:39]
	s_and_saveexec_b64 s[30:31], s[0:1]
	global_store_short v[32:33], v24, off
	s_mov_b64 exec, s[30:31]
	v_addc_co_u32_e64 v2, vcc, 0, v2, s[0:1]
	v_subb_co_u32_e64 v34, vcc, v34, 0, s[24:25]
	v_add_u32_e32 v24, 0x107, v30
	v_med3_i32 v35, v34, 0, 1
	v_sub_u32_e32 v35, v36, v35
	v_cmp_gt_i32_sdwa s[0:1], v27, v35 src0_sel:WORD_1 src1_sel:DWORD
	v_cmp_eq_u32_sdwa s[24:25], v27, v36 src0_sel:WORD_1 src1_sel:DWORD
	v_lshl_add_u64 v[26:27], v[2:3], 1, v[38:39]
	s_and_saveexec_b64 s[30:31], s[0:1]
	global_store_short v[26:27], v24, off
	s_mov_b64 exec, s[30:31]
	v_addc_co_u32_e64 v2, vcc, 0, v2, s[0:1]
	v_subb_co_u32_e64 v34, vcc, v34, 0, s[24:25]
	v_add_u32_e32 v24, 0x108, v30
	v_med3_i32 v35, v34, 0, 1
	v_sub_u32_e32 v35, v36, v35
	v_cmp_gt_i32_sdwa s[0:1], v20, v35 src0_sel:WORD_0 src1_sel:DWORD
	v_cmp_eq_u32_sdwa s[24:25], v20, v36 src0_sel:WORD_0 src1_sel:DWORD
	v_lshl_add_u64 v[26:27], v[2:3], 1, v[38:39]
	s_and_saveexec_b64 s[30:31], s[0:1]
	global_store_short v[26:27], v24, off
	s_mov_b64 exec, s[30:31]
	v_addc_co_u32_e64 v2, vcc, 0, v2, s[0:1]
	v_subb_co_u32_e64 v34, vcc, v34, 0, s[24:25]
	v_add_u32_e32 v24, 0x109, v30
	v_med3_i32 v35, v34, 0, 1
	v_sub_u32_e32 v35, v36, v35
	v_cmp_gt_i32_sdwa s[0:1], v20, v35 src0_sel:WORD_1 src1_sel:DWORD
	v_cmp_eq_u32_sdwa s[24:25], v20, v36 src0_sel:WORD_1 src1_sel:DWORD
	v_lshl_add_u64 v[26:27], v[2:3], 1, v[38:39]
	s_and_saveexec_b64 s[30:31], s[0:1]
	global_store_short v[26:27], v24, off
	s_mov_b64 exec, s[30:31]
	v_addc_co_u32_e64 v2, vcc, 0, v2, s[0:1]
	v_subb_co_u32_e64 v34, vcc, v34, 0, s[24:25]
	v_add_u32_e32 v24, 0x10a, v30
	v_med3_i32 v35, v34, 0, 1
	v_sub_u32_e32 v35, v36, v35
	v_cmp_gt_i32_sdwa s[0:1], v21, v35 src0_sel:WORD_0 src1_sel:DWORD
	v_cmp_eq_u32_sdwa s[24:25], v21, v36 src0_sel:WORD_0 src1_sel:DWORD
	v_lshl_add_u64 v[26:27], v[2:3], 1, v[38:39]
	s_and_saveexec_b64 s[30:31], s[0:1]
	global_store_short v[26:27], v24, off
	s_mov_b64 exec, s[30:31]
	v_addc_co_u32_e64 v2, vcc, 0, v2, s[0:1]
	v_subb_co_u32_e64 v34, vcc, v34, 0, s[24:25]
	v_add_u32_e32 v24, 0x10b, v30
	v_med3_i32 v35, v34, 0, 1
	v_sub_u32_e32 v35, v36, v35
	v_cmp_gt_i32_sdwa s[0:1], v21, v35 src0_sel:WORD_1 src1_sel:DWORD
	v_cmp_eq_u32_sdwa s[24:25], v21, v36 src0_sel:WORD_1 src1_sel:DWORD
	v_lshl_add_u64 v[20:21], v[2:3], 1, v[38:39]
	s_and_saveexec_b64 s[30:31], s[0:1]
	global_store_short v[20:21], v24, off
	s_mov_b64 exec, s[30:31]
	v_addc_co_u32_e64 v2, vcc, 0, v2, s[0:1]
	v_subb_co_u32_e64 v34, vcc, v34, 0, s[24:25]
	v_add_u32_e32 v20, 0x10c, v30
	v_med3_i32 v35, v34, 0, 1
	v_sub_u32_e32 v35, v36, v35
	v_cmp_gt_i32_sdwa s[0:1], v22, v35 src0_sel:WORD_0 src1_sel:DWORD
	v_cmp_eq_u32_sdwa s[24:25], v22, v36 src0_sel:WORD_0 src1_sel:DWORD
	v_lshl_add_u64 v[24:25], v[2:3], 1, v[38:39]
	s_and_saveexec_b64 s[30:31], s[0:1]
	global_store_short v[24:25], v20, off
	s_mov_b64 exec, s[30:31]
	v_addc_co_u32_e64 v2, vcc, 0, v2, s[0:1]
	v_subb_co_u32_e64 v34, vcc, v34, 0, s[24:25]
	v_add_u32_e32 v20, 0x10d, v30
	v_med3_i32 v35, v34, 0, 1
	v_sub_u32_e32 v35, v36, v35
	v_cmp_gt_i32_sdwa s[0:1], v22, v35 src0_sel:WORD_1 src1_sel:DWORD
	v_cmp_eq_u32_sdwa s[24:25], v22, v36 src0_sel:WORD_1 src1_sel:DWORD
	v_lshl_add_u64 v[24:25], v[2:3], 1, v[38:39]
	s_and_saveexec_b64 s[30:31], s[0:1]
	global_store_short v[24:25], v20, off
	s_mov_b64 exec, s[30:31]
	v_addc_co_u32_e64 v2, vcc, 0, v2, s[0:1]
	v_subb_co_u32_e64 v34, vcc, v34, 0, s[24:25]
	v_add_u32_e32 v20, 0x10e, v30
	v_med3_i32 v35, v34, 0, 1
	v_sub_u32_e32 v35, v36, v35
	v_cmp_gt_i32_sdwa s[0:1], v23, v35 src0_sel:WORD_0 src1_sel:DWORD
	v_cmp_eq_u32_sdwa s[24:25], v23, v36 src0_sel:WORD_0 src1_sel:DWORD
	v_lshl_add_u64 v[24:25], v[2:3], 1, v[38:39]
	s_and_saveexec_b64 s[30:31], s[0:1]
	global_store_short v[24:25], v20, off
	s_mov_b64 exec, s[30:31]
	v_addc_co_u32_e64 v2, vcc, 0, v2, s[0:1]
	v_subb_co_u32_e64 v34, vcc, v34, 0, s[24:25]
	v_med3_i32 v35, v34, 0, 1
	v_sub_u32_e32 v35, v36, v35
	v_cmp_gt_i32_sdwa s[24:25], v23, v35 src0_sel:WORD_1 src1_sel:DWORD
	v_lshl_add_u64 v[20:21], v[2:3], 1, v[38:39]
	v_or_b32_e32 v35, 15, v28
	s_and_saveexec_b64 s[30:31], s[24:25]
	global_store_short v[20:21], v35, off
	s_mov_b64 exec, s[30:31]
.LBB0_971:
.LBB0_972:
.LBB0_973:
	s_or_b64 exec, exec, s[18:19]
	s_andn2_b64 vcc, exec, s[28:29]
	s_cbranch_vccz .LBB0_976

.LBB0_976:
	ds_read_u16 v2, v50 offset:36928
	s_waitcnt lgkmcnt(0)
	v_cmp_ne_u16_e32 vcc, 0, v2
	s_and_saveexec_b64 s[18:19], vcc
	s_cbranch_execz .LBB0_1103
	ds_read_u16 v2, v49 offset:36928
	s_waitcnt vmcnt(5)
	v_add_u32_e32 v20, 0x11240, v49
	ds_read_b32 v20, v20
	v_lshl_add_u64 v[22:23], v[40:41], 0, s[16:17]
	s_mov_b64 s[0:1], 0x200
	s_waitcnt lgkmcnt(1)
	v_lshrrev_b32_e32 v21, 8, v2
	v_and_b32_e32 v2, 0xff, v2
	v_cndmask_b32_e64 v21, v21, 0, s[22:23]
	v_cndmask_b32_e64 v2, v2, 0, s[22:23]
	s_waitcnt vmcnt(4) lgkmcnt(0)
	v_add_u32_sdwa v26, v21, v20 dst_sel:DWORD dst_unused:UNUSED_PAD src0_sel:DWORD src1_sel:WORD_1
	v_add_u32_sdwa v27, v2, v20 dst_sel:DWORD dst_unused:UNUSED_PAD src0_sel:DWORD src1_sel:WORD_0
	v_lshl_add_u64 v[20:21], v[22:23], 0, s[0:1]
	s_waitcnt vmcnt(2)
	v_min_i32_e32 v2, v26, v37
	v_add_u32_e32 v2, v2, v27
	v_sub_u32_e32 v26, v37, v26
	v_med3_i32 v27, v26, 0, 1
	v_sub_u32_e32 v27, v36, v27
	v_cmp_gt_i32_sdwa s[0:1], v16, v27 src0_sel:WORD_0 src1_sel:DWORD
	v_cmp_eq_u32_sdwa s[24:25], v16, v36 src0_sel:WORD_0 src1_sel:DWORD
	v_lshl_add_u64 v[24:25], v[2:3], 1, v[38:39]
	s_and_saveexec_b64 s[28:29], s[0:1]
	global_store_short v[24:25], v20, off
	s_mov_b64 exec, s[28:29]
	v_addc_co_u32_e64 v2, vcc, 0, v2, s[0:1]
	v_subb_co_u32_e64 v26, vcc, v26, 0, s[24:25]
	v_add_u32_e32 v24, 0x201, v22
	v_med3_i32 v27, v26, 0, 1
	v_sub_u32_e32 v27, v36, v27
	v_cmp_gt_i32_sdwa s[0:1], v16, v27 src0_sel:WORD_1 src1_sel:DWORD
	v_cmp_eq_u32_sdwa s[24:25], v16, v36 src0_sel:WORD_1 src1_sel:DWORD
	v_lshl_add_u64 v[28:29], v[2:3], 1, v[38:39]
	s_and_saveexec_b64 s[28:29], s[0:1]
	global_store_short v[28:29], v24, off
	s_mov_b64 exec, s[28:29]
	v_addc_co_u32_e64 v2, vcc, 0, v2, s[0:1]
	v_subb_co_u32_e64 v26, vcc, v26, 0, s[24:25]
	v_add_u32_e32 v24, 0x202, v22
	v_med3_i32 v27, v26, 0, 1
	v_sub_u32_e32 v27, v36, v27
	v_cmp_gt_i32_sdwa s[0:1], v17, v27 src0_sel:WORD_0 src1_sel:DWORD
	v_cmp_eq_u32_sdwa s[24:25], v17, v36 src0_sel:WORD_0 src1_sel:DWORD
	v_lshl_add_u64 v[28:29], v[2:3], 1, v[38:39]
	s_and_saveexec_b64 s[28:29], s[0:1]
	global_store_short v[28:29], v24, off
	s_mov_b64 exec, s[28:29]
	v_addc_co_u32_e64 v2, vcc, 0, v2, s[0:1]
	v_subb_co_u32_e64 v26, vcc, v26, 0, s[24:25]
	v_add_u32_e32 v24, 0x203, v22
	v_med3_i32 v27, v26, 0, 1
	v_sub_u32_e32 v27, v36, v27
	v_cmp_gt_i32_sdwa s[0:1], v17, v27 src0_sel:WORD_1 src1_sel:DWORD
	v_cmp_eq_u32_sdwa s[24:25], v17, v36 src0_sel:WORD_1 src1_sel:DWORD
	v_lshl_add_u64 v[16:17], v[2:3], 1, v[38:39]
	s_and_saveexec_b64 s[28:29], s[0:1]
	global_store_short v[16:17], v24, off
	s_mov_b64 exec, s[28:29]
	v_addc_co_u32_e64 v2, vcc, 0, v2, s[0:1]
	v_subb_co_u32_e64 v26, vcc, v26, 0, s[24:25]
	v_add_u32_e32 v16, 0x204, v22
	v_med3_i32 v27, v26, 0, 1
	v_sub_u32_e32 v27, v36, v27
	v_cmp_gt_i32_sdwa s[0:1], v18, v27 src0_sel:WORD_0 src1_sel:DWORD
	v_cmp_eq_u32_sdwa s[24:25], v18, v36 src0_sel:WORD_0 src1_sel:DWORD
	v_lshl_add_u64 v[24:25], v[2:3], 1, v[38:39]
	s_and_saveexec_b64 s[28:29], s[0:1]
	global_store_short v[24:25], v16, off
	s_mov_b64 exec, s[28:29]
	v_addc_co_u32_e64 v2, vcc, 0, v2, s[0:1]
	v_subb_co_u32_e64 v26, vcc, v26, 0, s[24:25]
	v_add_u32_e32 v16, 0x205, v22
	v_med3_i32 v27, v26, 0, 1
	v_sub_u32_e32 v27, v36, v27
	v_cmp_gt_i32_sdwa s[0:1], v18, v27 src0_sel:WORD_1 src1_sel:DWORD
	v_cmp_eq_u32_sdwa s[24:25], v18, v36 src0_sel:WORD_1 src1_sel:DWORD
	v_lshl_add_u64 v[24:25], v[2:3], 1, v[38:39]
	s_and_saveexec_b64 s[28:29], s[0:1]
	global_store_short v[24:25], v16, off
	s_mov_b64 exec, s[28:29]
	v_addc_co_u32_e64 v2, vcc, 0, v2, s[0:1]
	v_subb_co_u32_e64 v26, vcc, v26, 0, s[24:25]
	v_add_u32_e32 v16, 0x206, v22
	v_med3_i32 v27, v26, 0, 1
	v_sub_u32_e32 v27, v36, v27
	v_cmp_gt_i32_sdwa s[0:1], v19, v27 src0_sel:WORD_0 src1_sel:DWORD
	v_cmp_eq_u32_sdwa s[24:25], v19, v36 src0_sel:WORD_0 src1_sel:DWORD
	v_lshl_add_u64 v[24:25], v[2:3], 1, v[38:39]
	s_and_saveexec_b64 s[28:29], s[0:1]
	global_store_short v[24:25], v16, off
	s_mov_b64 exec, s[28:29]
	v_addc_co_u32_e64 v2, vcc, 0, v2, s[0:1]
	v_subb_co_u32_e64 v26, vcc, v26, 0, s[24:25]
	v_add_u32_e32 v16, 0x207, v22
	v_med3_i32 v27, v26, 0, 1
	v_sub_u32_e32 v27, v36, v27
	v_cmp_gt_i32_sdwa s[0:1], v19, v27 src0_sel:WORD_1 src1_sel:DWORD
	v_cmp_eq_u32_sdwa s[24:25], v19, v36 src0_sel:WORD_1 src1_sel:DWORD
	v_lshl_add_u64 v[18:19], v[2:3], 1, v[38:39]
	s_and_saveexec_b64 s[28:29], s[0:1]
	global_store_short v[18:19], v16, off
	s_mov_b64 exec, s[28:29]
	v_addc_co_u32_e64 v2, vcc, 0, v2, s[0:1]
	v_subb_co_u32_e64 v26, vcc, v26, 0, s[24:25]
	v_add_u32_e32 v16, 0x208, v22
	v_med3_i32 v27, v26, 0, 1
	v_sub_u32_e32 v27, v36, v27
	v_cmp_gt_i32_sdwa s[0:1], v12, v27 src0_sel:WORD_0 src1_sel:DWORD
	v_cmp_eq_u32_sdwa s[24:25], v12, v36 src0_sel:WORD_0 src1_sel:DWORD
	v_lshl_add_u64 v[18:19], v[2:3], 1, v[38:39]
	s_and_saveexec_b64 s[28:29], s[0:1]
	global_store_short v[18:19], v16, off
	s_mov_b64 exec, s[28:29]
	v_addc_co_u32_e64 v2, vcc, 0, v2, s[0:1]
	v_subb_co_u32_e64 v26, vcc, v26, 0, s[24:25]
	v_add_u32_e32 v16, 0x209, v22
	v_med3_i32 v27, v26, 0, 1
	v_sub_u32_e32 v27, v36, v27
	v_cmp_gt_i32_sdwa s[0:1], v12, v27 src0_sel:WORD_1 src1_sel:DWORD
	v_cmp_eq_u32_sdwa s[24:25], v12, v36 src0_sel:WORD_1 src1_sel:DWORD
	v_lshl_add_u64 v[18:19], v[2:3], 1, v[38:39]
	s_and_saveexec_b64 s[28:29], s[0:1]
	global_store_short v[18:19], v16, off
	s_mov_b64 exec, s[28:29]
	v_addc_co_u32_e64 v2, vcc, 0, v2, s[0:1]
	v_subb_co_u32_e64 v26, vcc, v26, 0, s[24:25]
	v_add_u32_e32 v16, 0x20a, v22
	v_med3_i32 v27, v26, 0, 1
	v_sub_u32_e32 v27, v36, v27
	v_cmp_gt_i32_sdwa s[0:1], v13, v27 src0_sel:WORD_0 src1_sel:DWORD
	v_cmp_eq_u32_sdwa s[24:25], v13, v36 src0_sel:WORD_0 src1_sel:DWORD
	v_lshl_add_u64 v[18:19], v[2:3], 1, v[38:39]
	s_and_saveexec_b64 s[28:29], s[0:1]
	global_store_short v[18:19], v16, off
	s_mov_b64 exec, s[28:29]
	v_addc_co_u32_e64 v2, vcc, 0, v2, s[0:1]
	v_subb_co_u32_e64 v26, vcc, v26, 0, s[24:25]
	v_add_u32_e32 v16, 0x20b, v22
	v_med3_i32 v27, v26, 0, 1
	v_sub_u32_e32 v27, v36, v27
	v_cmp_gt_i32_sdwa s[0:1], v13, v27 src0_sel:WORD_1 src1_sel:DWORD
	v_cmp_eq_u32_sdwa s[24:25], v13, v36 src0_sel:WORD_1 src1_sel:DWORD
	v_lshl_add_u64 v[12:13], v[2:3], 1, v[38:39]
	s_and_saveexec_b64 s[28:29], s[0:1]
	global_store_short v[12:13], v16, off
	s_mov_b64 exec, s[28:29]
	v_addc_co_u32_e64 v2, vcc, 0, v2, s[0:1]
	v_subb_co_u32_e64 v26, vcc, v26, 0, s[24:25]
	v_add_u32_e32 v12, 0x20c, v22
	v_med3_i32 v27, v26, 0, 1
	v_sub_u32_e32 v27, v36, v27
	v_cmp_gt_i32_sdwa s[0:1], v14, v27 src0_sel:WORD_0 src1_sel:DWORD
	v_cmp_eq_u32_sdwa s[24:25], v14, v36 src0_sel:WORD_0 src1_sel:DWORD
	v_lshl_add_u64 v[16:17], v[2:3], 1, v[38:39]
	s_and_saveexec_b64 s[28:29], s[0:1]
	global_store_short v[16:17], v12, off
	s_mov_b64 exec, s[28:29]
	v_addc_co_u32_e64 v2, vcc, 0, v2, s[0:1]
	v_subb_co_u32_e64 v26, vcc, v26, 0, s[24:25]
	v_add_u32_e32 v12, 0x20d, v22
	v_med3_i32 v27, v26, 0, 1
	v_sub_u32_e32 v27, v36, v27
	v_cmp_gt_i32_sdwa s[0:1], v14, v27 src0_sel:WORD_1 src1_sel:DWORD
	v_cmp_eq_u32_sdwa s[24:25], v14, v36 src0_sel:WORD_1 src1_sel:DWORD
	v_lshl_add_u64 v[16:17], v[2:3], 1, v[38:39]
	s_and_saveexec_b64 s[28:29], s[0:1]
	global_store_short v[16:17], v12, off
	s_mov_b64 exec, s[28:29]
	v_addc_co_u32_e64 v2, vcc, 0, v2, s[0:1]
	v_subb_co_u32_e64 v26, vcc, v26, 0, s[24:25]
	v_add_u32_e32 v12, 0x20e, v22
	v_med3_i32 v27, v26, 0, 1
	v_sub_u32_e32 v27, v36, v27
	v_cmp_gt_i32_sdwa s[0:1], v15, v27 src0_sel:WORD_0 src1_sel:DWORD
	v_cmp_eq_u32_sdwa s[24:25], v15, v36 src0_sel:WORD_0 src1_sel:DWORD
	v_lshl_add_u64 v[16:17], v[2:3], 1, v[38:39]
	s_and_saveexec_b64 s[28:29], s[0:1]
	global_store_short v[16:17], v12, off
	s_mov_b64 exec, s[28:29]
	v_addc_co_u32_e64 v2, vcc, 0, v2, s[0:1]
	v_subb_co_u32_e64 v26, vcc, v26, 0, s[24:25]
	v_med3_i32 v27, v26, 0, 1
	v_sub_u32_e32 v27, v36, v27
	v_cmp_gt_i32_sdwa s[24:25], v15, v27 src0_sel:WORD_1 src1_sel:DWORD
	v_lshl_add_u64 v[12:13], v[2:3], 1, v[38:39]
	v_or_b32_e32 v27, 15, v20
	s_and_saveexec_b64 s[28:29], s[24:25]
	global_store_short v[12:13], v27, off
	s_mov_b64 exec, s[28:29]
.LBB0_1101:
.LBB0_1102:
.LBB0_1103:
	s_or_b64 exec, exec, s[18:19]
	s_andn2_b64 vcc, exec, s[26:27]
	s_cbranch_vccnz .LBB0_711
